# speedup vs baseline: 1.0926x; 1.0726x over previous
_Z10snn_kernel6Params:
	s_load_dwordx16 s[44:59], s[0:1], 0x0
	s_load_dwordx8 s[60:67], s[0:1], 0x40
	s_load_dwordx2 s[72:73], s[0:1], 0x60
	v_and_b32_e32 v98, 0x3ff, v0
	s_lshr_b32 s33, s2, 3
	s_and_b32 s75, s2, 7
	s_lshl_b32 s3, s33, 4
	v_and_b32_e32 v73, 63, v98
	v_lshrrev_b32_e32 v72, 4, v98
	v_and_b32_e32 v70, 15, v98
	v_and_b32_e32 v75, 15, v72
	v_lshlrev_b32_e32 v74, 4, v98
	v_and_b32_e32 v63, 31, v98
	v_readfirstlane_b32 s76, v98
	s_mul_i32 s74, s75, 48
	s_lshl_b32 s79, s75, 5
	s_add_i32 s78, s79, s33
	s_mov_b32 s68, 0
	s_movk_i32 s6, 0xff
	v_cmp_lt_u32_e64 s[42:43], s6, v98
	v_cmp_eq_u32_e64 s[4:5], 0, v73
	v_cmp_eq_u32_e64 s[8:9], 0, v63
	v_mov_b32_e32 v34, 0
	s_lshr_b32 s10, s76, 6
	s_waitcnt lgkmcnt(0)
	v_or_b32_e32 v252, s3, v75
	s_lshl_b32 s82, s75, 9
	v_add_u32_e32 v253, s82, v252
	v_lshlrev_b32_e32 v252, 2, v252
	v_lshlrev_b32_e32 v253, 2, v253
	v_and_b32_e32 v161, 0xff, v98
	v_lshlrev_b32_e32 v161, 2, v161
	global_load_dword v252, v252, s[56:57]
	global_load_dword v253, v253, s[58:59]
	global_load_dword v162, v161, s[50:51] offset:1024
	global_load_dword v161, v161, s[50:51]
	v_add_u32_e32 v0, s74, v72
	v_lshlrev_b32_e32 v0, 9, v0
	v_add3_u32 v0, v0, s3, v70
	v_lshlrev_b32_e32 v0, 2, v0
	global_load_dword v67, v0, s[44:45]
	v_add_u32_e32 v1, 0x10000, v0
	s_cmp_gt_u32 s10, 3
	s_cbranch_scc1 .Lco_noin1
	global_load_dword v68, v1, s[44:45]
.Lco_noin1:
	s_lshl_b32 s11, s75, 6
	v_add_u32_e32 v69, s11, v73
	s_lshl_b32 s12, s10, 1
	s_add_i32 s13, s3, s12
	v_lshl_add_u32 v0, v69, 9, s13
	v_lshlrev_b32_e32 v0, 2, v0
	v_add_u32_e32 v1, 0x100000, v0
	v_add_u32_e32 v2, 0x200000, v0
	v_lshlrev_b32_e32 v3, 2, v69
	global_load_dwordx2 v[36:37], v0, s[46:47]
	global_load_dwordx2 v[38:39], v0, s[62:63]
	global_load_dwordx2 v[40:41], v1, s[62:63]
	global_load_dwordx2 v[42:43], v2, s[62:63]
	global_load_dwordx2 v[44:45], v0, s[52:53]
	global_load_dwordx2 v[46:47], v0, s[54:55]
	global_load_dword v48, v3, s[60:61]
	v_cmp_gt_u32_e32 vcc, 4, v98
	s_and_saveexec_b64 s[14:15], vcc
	v_mov_b32_e32 v4, 0x26c10
	v_lshl_add_u32 v4, v98, 2, v4
	ds_write_b32 v4, v34
	s_mov_b64 exec, s[14:15]
	v_cmp_eq_u32_e32 vcc, 0, v98
	s_and_saveexec_b64 s[14:15], vcc
	v_mov_b32_e32 v4, 0x26c00
	ds_write2_b32 v4, v34, v34 offset1:1
	s_mov_b64 exec, s[14:15]
	v_mov_b32_e32 v159, 0
	v_mov_b32_e32 v9, 0
	v_mov_b32_e32 v18, 0
	v_mov_b32_e32 v129, 0
	v_mov_b32_e32 v130, 0
	v_mov_b32_e32 v71, 0
	v_mov_b32_e32 v158, 0
	v_mov_b32_e32 v131, 0
	v_mov_b32_e32 v19, 0
	v_mov_b32_e32 v132, 0
	v_mov_b32_e32 v133, 0
	v_mov_b32_e32 v81, 0
	v_mov_b32_e32 v157, 0
	v_mov_b32_e32 v134, 0
	v_mov_b32_e32 v20, 0
	v_mov_b32_e32 v135, 0
	v_mov_b32_e32 v136, 0
	v_mov_b32_e32 v85, 0
	v_mov_b32_e32 v156, 0
	v_mov_b32_e32 v137, 0
	v_mov_b32_e32 v21, 0
	v_mov_b32_e32 v138, 0
	v_mov_b32_e32 v139, 0
	v_mov_b32_e32 v86, 0
	v_mov_b32_e32 v155, 0
	v_mov_b32_e32 v140, 0
	v_mov_b32_e32 v22, 0
	v_mov_b32_e32 v141, 0
	v_mov_b32_e32 v142, 0
	v_mov_b32_e32 v87, 0
	v_mov_b32_e32 v154, 0
	v_mov_b32_e32 v143, 0
	v_mov_b32_e32 v23, 0
	v_mov_b32_e32 v144, 0
	v_mov_b32_e32 v145, 0
	v_mov_b32_e32 v88, 0
	v_mov_b32_e32 v153, 0
	v_mov_b32_e32 v146, 0
	v_mov_b32_e32 v24, 0
	v_mov_b32_e32 v147, 0
	v_mov_b32_e32 v148, 0
	v_mov_b32_e32 v89, 0
	v_mov_b32_e32 v149, 0
	v_mov_b32_e32 v150, 0
	v_mov_b32_e32 v25, 0
	v_mov_b32_e32 v151, 0
	v_mov_b32_e32 v152, 0
	v_mov_b32_e32 v90, 0
	v_mov_b32_e32 v128, 0
	v_mov_b32_e32 v121, 0
	v_mov_b32_e32 v26, 0
	v_mov_b32_e32 v123, 0
	v_mov_b32_e32 v125, 0
	v_mov_b32_e32 v91, 0
	v_mov_b32_e32 v127, 0
	v_mov_b32_e32 v122, 0
	v_mov_b32_e32 v27, 0
	v_mov_b32_e32 v124, 0
	v_mov_b32_e32 v126, 0
	v_mov_b32_e32 v92, 0
	v_mov_b32_e32 v120, 0
	v_mov_b32_e32 v112, 0
	v_mov_b32_e32 v28, 0
	v_mov_b32_e32 v115, 0
	v_mov_b32_e32 v117, 0
	v_mov_b32_e32 v93, 0
	v_mov_b32_e32 v119, 0
	v_mov_b32_e32 v113, 0
	v_mov_b32_e32 v29, 0
	v_mov_b32_e32 v116, 0
	v_mov_b32_e32 v118, 0
	v_mov_b32_e32 v94, 0
	v_mov_b32_e32 v114, 0
	v_mov_b32_e32 v100, 0
	v_mov_b32_e32 v30, 0
	v_mov_b32_e32 v103, 0
	v_mov_b32_e32 v107, 0
	v_mov_b32_e32 v95, 0
	v_mov_b32_e32 v111, 0
	v_mov_b32_e32 v101, 0
	v_mov_b32_e32 v31, 0
	v_mov_b32_e32 v104, 0
	v_mov_b32_e32 v108, 0
	v_mov_b32_e32 v96, 0
	v_mov_b32_e32 v17, 0
	v_mov_b32_e32 v102, 0
	v_mov_b32_e32 v32, 0
	v_mov_b32_e32 v105, 0
	v_mov_b32_e32 v109, 0
	v_mov_b32_e32 v97, 0
	v_mov_b32_e32 v8, 0
	v_mov_b32_e32 v16, 0
	v_mov_b32_e32 v33, 0
	v_mov_b32_e32 v106, 0
	v_mov_b32_e32 v110, 0
	v_mov_b32_e32 v99, 0
	s_waitcnt vmcnt(0)
	s_movk_i32 s84, 0x1000
	s_mov_b64 s[34:35], 0
	v_mul_f32_e64 v50, v48, |v36|
	v_cmp_neq_f32_e64 s[16:17], 0, v38
	v_cmp_neq_f32_e64 s[18:19], 0, v40
	v_cmp_neq_f32_e64 s[20:21], 0, v42
	v_cmp_neq_f32_e64 s[22:23], 0, v50
	v_cndmask_b32_e64 v51, v42, v40, s[18:19]
	v_cndmask_b32_e64 v52, 2, 1, s[18:19]
	v_cndmask_b32_e64 v51, v51, v38, s[16:17]
	v_cndmask_b32_e64 v52, v52, 0, s[16:17]
	s_or_b64 s[24:25], s[16:17], s[18:19]
	s_and_b64 s[28:29], s[16:17], s[18:19]
	s_and_b64 s[30:31], s[24:25], s[20:21]
	s_or_b64 s[24:25], s[24:25], s[20:21]
	s_or_b64 s[28:29], s[28:29], s[30:31]
	s_and_b64 s[26:27], s[22:23], s[24:25]
	s_and_b64 s[28:29], s[28:29], s[22:23]
	s_or_b64 s[34:35], s[34:35], s[28:29]
	v_lshlrev_b32_e64 v53, v52, s84
	v_lshlrev_b32_e32 v54, 3, v69
	v_sub_u32_e32 v54, v54, v53
	v_and_b32_e32 v56, 0xffff, v54
	v_mul_f32_e32 v57, v50, v51
	v_mul_f32_e32 v58, v44, v51
	v_mul_f32_e32 v59, v46, v51
	v_and_b32_e32 v55, 0x7fffffff, v50
	v_div_scale_f32 v61, s[30:31], v55, v55, 2.0
	v_rcp_f32_e32 v62, v61
	v_div_scale_f32 v55, vcc, 2.0, v55, 2.0
	v_fma_f32 v53, -v61, v62, 1.0
	v_fmac_f32_e32 v62, v53, v62
	v_mul_f32_e32 v53, v55, v62
	v_fma_f32 v54, -v61, v53, v55
	v_fmac_f32_e32 v53, v54, v62
	v_fma_f32 v55, -v61, v53, v55
	v_div_fmas_f32 v55, v55, v62, v53
	v_div_fixup_f32 v60, v55, |v50|, 2.0
	v_mbcnt_lo_u32_b32 v53, s26, 0
	v_mbcnt_hi_u32_b32 v53, s27, v53
	s_bcnt1_i32_b64 s85, s[26:27]
	s_add_i32 s36, s13, 0
	s_lshl_b32 s36, s36, 3
	s_add_i32 s87, s36, s75
	s_lshl_b32 s37, s87, 11
	s_add_i32 s37, s37, 0x800000
	v_lshl_add_u32 v4, v53, 5, s37
	s_and_saveexec_b64 s[38:39], s[26:27]
	s_cbranch_execz .Lco_nost0
	global_store_dwordx4 v4, v[56:59], s[66:67] sc1
	global_store_dword v4, v60, s[66:67] offset:16 sc1
.Lco_nost0:
	s_mov_b64 exec, s[38:39]
	v_mul_f32_e64 v50, v48, |v37|
	v_cmp_neq_f32_e64 s[16:17], 0, v39
	v_cmp_neq_f32_e64 s[18:19], 0, v41
	v_cmp_neq_f32_e64 s[20:21], 0, v43
	v_cmp_neq_f32_e64 s[22:23], 0, v50
	v_cndmask_b32_e64 v51, v43, v41, s[18:19]
	v_cndmask_b32_e64 v52, 2, 1, s[18:19]
	v_cndmask_b32_e64 v51, v51, v39, s[16:17]
	v_cndmask_b32_e64 v52, v52, 0, s[16:17]
	s_or_b64 s[24:25], s[16:17], s[18:19]
	s_and_b64 s[28:29], s[16:17], s[18:19]
	s_and_b64 s[30:31], s[24:25], s[20:21]
	s_or_b64 s[24:25], s[24:25], s[20:21]
	s_or_b64 s[28:29], s[28:29], s[30:31]
	s_and_b64 s[26:27], s[22:23], s[24:25]
	s_and_b64 s[28:29], s[28:29], s[22:23]
	s_or_b64 s[34:35], s[34:35], s[28:29]
	v_lshlrev_b32_e64 v53, v52, s84
	v_lshlrev_b32_e32 v54, 3, v69
	v_sub_u32_e32 v54, v54, v53
	v_and_b32_e32 v76, 0xffff, v54
	v_mul_f32_e32 v77, v50, v51
	v_mul_f32_e32 v78, v45, v51
	v_mul_f32_e32 v79, v47, v51
	v_and_b32_e32 v55, 0x7fffffff, v50
	v_div_scale_f32 v61, s[30:31], v55, v55, 2.0
	v_rcp_f32_e32 v62, v61
	v_div_scale_f32 v55, vcc, 2.0, v55, 2.0
	v_fma_f32 v53, -v61, v62, 1.0
	v_fmac_f32_e32 v62, v53, v62
	v_mul_f32_e32 v53, v55, v62
	v_fma_f32 v54, -v61, v53, v55
	v_fmac_f32_e32 v53, v54, v62
	v_fma_f32 v55, -v61, v53, v55
	v_div_fmas_f32 v55, v55, v62, v53
	v_div_fixup_f32 v80, v55, |v50|, 2.0
	v_mbcnt_lo_u32_b32 v53, s26, 0
	v_mbcnt_hi_u32_b32 v53, s27, v53
	s_bcnt1_i32_b64 s86, s[26:27]
	s_add_i32 s36, s13, 1
	s_lshl_b32 s36, s36, 3
	s_add_i32 s88, s36, s75
	s_lshl_b32 s37, s88, 11
	s_add_i32 s37, s37, 0x800000
	v_lshl_add_u32 v5, v53, 5, s37
	s_and_saveexec_b64 s[38:39], s[26:27]
	s_cbranch_execz .Lco_nost1
	global_store_dwordx4 v5, v[76:79], s[66:67] sc1
	global_store_dword v5, v80, s[66:67] offset:16 sc1
.Lco_nost1:
	s_mov_b64 exec, s[38:39]
	v_mov_b32_e32 v0, 0x24400
	v_lshl_add_u32 v0, v98, 2, v0
	ds_write_b32 v0, v67
	s_cmp_gt_u32 s10, 3
	s_cbranch_scc1 .Lco_noin2
	ds_write_b32 v0, v68 offset:2048
.Lco_noin2:
	s_waitcnt vmcnt(0)
	s_cmp_lg_u64 s[34:35], 0
	s_cselect_b32 s36, 0x8000, 0
	s_or_b32 s36, s36, 0x5c3a0000
	s_or_b32 s85, s85, s36
	s_or_b32 s86, s86, s36
	s_lshl_b32 s87, s87, 7
	s_lshl_b32 s88, s88, 7
	s_add_i32 s87, s87, 0x600000
	s_add_i32 s88, s88, 0x600000
	s_and_saveexec_b64 s[38:39], s[4:5]
	s_cbranch_execz .Lco_nocnt
	v_mov_b32_e32 v0, s87
	v_mov_b32_e32 v1, s85
	v_mov_b32_e32 v2, s88
	v_mov_b32_e32 v3, s86
	global_store_dword v0, v1, s[66:67] sc1
	global_store_dword v2, v3, s[66:67] sc1
.Lco_nocnt:
	s_mov_b64 exec, s[38:39]
	s_cmp_gt_u32 s10, 1
	s_cbranch_scc1 .Lco_nopoll
	s_lshl_b32 s36, s33, 7
	v_add_u32_e32 v0, s36, v98
	v_lshlrev_b32_e32 v0, 7, v0
	v_add_u32_e32 v0, 0x600000, v0
	s_mov_b32 s37, 0
.Lco_poll:
	global_load_dword v1, v0, s[66:67] sc1
	s_waitcnt vmcnt(0)
	v_lshrrev_b32_e32 v2, 16, v1
	v_cmp_ne_u32_e32 vcc, 0x5c3a, v2
	s_add_i32 s37, s37, 1
	s_nop 0
	s_cbranch_vccz .Lco_polled
	s_cmp_lt_u32 s37, 0x40000
	s_cbranch_scc1 .Lco_poll
.Lco_polled:
	v_mov_b32_e32 v2, 0x26400
	v_lshl_add_u32 v2, v98, 2, v2
	ds_write_b32 v2, v1
.Lco_nopoll:
	s_waitcnt lgkmcnt(0)
	s_barrier
	v_mov_b32_e32 v0, 0x26400
	v_lshl_add_u32 v0, v75, 5, v0
	ds_read_b128 v[36:39], v0
	ds_read_b128 v[40:43], v0 offset:16
	s_waitcnt lgkmcnt(0)
	v_or3_b32 v44, v36, v37, v38
	v_or3_b32 v44, v44, v39, v40
	v_or3_b32 v44, v44, v41, v42
	v_or_b32_e32 v44, v44, v43
	v_bfe_u32 v44, v44, 15, 1
	v_and_b32_e32 v36, 0x7f, v36
	v_and_b32_e32 v37, 0x7f, v37
	v_and_b32_e32 v38, 0x7f, v38
	v_and_b32_e32 v39, 0x7f, v39
	v_and_b32_e32 v40, 0x7f, v40
	v_and_b32_e32 v41, 0x7f, v41
	v_and_b32_e32 v42, 0x7f, v42
	v_and_b32_e32 v43, 0x7f, v43
	v_mov_b32_e32 v45, v36
	v_add_u32_e32 v46, v45, v37
	v_add_u32_e32 v47, v46, v38
	v_add_u32_e32 v48, v47, v39
	v_add_u32_e32 v49, v48, v40
	v_add_u32_e32 v50, v49, v41
	v_add_u32_e32 v51, v50, v42
	v_add_u32_e32 v52, v51, v43
	v_cmp_lt_u32_e32 vcc, 0x100, v52
	v_add_u32_e32 v53, 15, v52
	v_lshrrev_b32_e32 v53, 4, v53
	v_cndmask_b32_e64 v54, 0, 1, vcc
	v_or_b32_e32 v44, v44, v54
	v_mov_b32_e32 v55, 0x26c00
	ds_max_u32 v55, v53
	ds_or_b32 v55, v44 offset:4
	s_waitcnt lgkmcnt(0)
	s_barrier
	ds_read_b64 v[0:1], v55
	v_lshlrev_b32_e32 v56, 5, v45
	v_lshlrev_b32_e32 v57, 5, v46
	v_lshlrev_b32_e32 v58, 5, v47
	v_lshlrev_b32_e32 v59, 5, v48
	v_lshlrev_b32_e32 v60, 5, v49
	v_lshlrev_b32_e32 v61, 5, v50
	v_lshlrev_b32_e32 v62, 5, v51
	v_sub_u32_e32 v56, 0x800, v56
	v_sub_u32_e32 v57, 0x1000, v57
	v_sub_u32_e32 v58, 0x1800, v58
	v_sub_u32_e32 v59, 0x2000, v59
	v_sub_u32_e32 v60, 0x2800, v60
	v_sub_u32_e32 v61, 0x3000, v61
	v_sub_u32_e32 v62, 0x3800, v62
	v_add_u32_e32 v63, s3, v75
	v_lshlrev_b32_e32 v63, 14, v63
	v_add_u32_e32 v63, 0x800000, v63
	s_waitcnt lgkmcnt(0)
	v_readfirstlane_b32 s77, v0
	v_readfirstlane_b32 s36, v1
	s_cmp_lg_u32 s36, 0
	s_cselect_b64 s[6:7], 0, -1
	s_cmp_gt_u32 s10, 3
	s_cbranch_scc1 .Lco_done
	s_cmp_lg_u32 s36, 0
	s_cbranch_scc1 .Lco_gen
	v_mov_b32_e32 v0, v70
	v_cmp_lt_u32_e64 s[12:13], v0, v52
	v_cmp_le_u32_e64 s[16:17], v45, v0
	v_cmp_le_u32_e64 s[18:19], v46, v0
	v_cmp_le_u32_e64 s[20:21], v47, v0
	v_cmp_le_u32_e64 s[22:23], v48, v0
	v_cmp_le_u32_e64 s[24:25], v49, v0
	v_cmp_le_u32_e64 s[26:27], v50, v0
	v_cmp_le_u32_e64 s[28:29], v51, v0
	v_cndmask_b32_e64 v1, 0, v56, s[16:17]
	v_cndmask_b32_e64 v1, v1, v57, s[18:19]
	v_cndmask_b32_e64 v1, v1, v58, s[20:21]
	v_cndmask_b32_e64 v1, v1, v59, s[22:23]
	v_cndmask_b32_e64 v1, v1, v60, s[24:25]
	v_cndmask_b32_e64 v1, v1, v61, s[26:27]
	v_cndmask_b32_e64 v1, v1, v62, s[28:29]
	v_lshl_add_u32 v2, v0, 5, v63
	v_add_u32_e32 v2, v2, v1
	s_and_saveexec_b64 s[30:31], s[12:13]
	s_cbranch_execz .Lco_nold0
	global_load_dwordx4 v[208:211], v2, s[66:67] sc1
	global_load_dword v71, v2, s[66:67] offset:16 sc1
	v_mov_b32_e32 v18, 1.0
.Lco_nold0:
	s_mov_b64 exec, s[30:31]
	v_add_u32_e32 v0, 16, v70
	v_cmp_lt_u32_e64 s[12:13], v0, v52
	v_cmp_le_u32_e64 s[16:17], v45, v0
	v_cmp_le_u32_e64 s[18:19], v46, v0
	v_cmp_le_u32_e64 s[20:21], v47, v0
	v_cmp_le_u32_e64 s[22:23], v48, v0
	v_cmp_le_u32_e64 s[24:25], v49, v0
	v_cmp_le_u32_e64 s[26:27], v50, v0
	v_cmp_le_u32_e64 s[28:29], v51, v0
	v_cndmask_b32_e64 v1, 0, v56, s[16:17]
	v_cndmask_b32_e64 v1, v1, v57, s[18:19]
	v_cndmask_b32_e64 v1, v1, v58, s[20:21]
	v_cndmask_b32_e64 v1, v1, v59, s[22:23]
	v_cndmask_b32_e64 v1, v1, v60, s[24:25]
	v_cndmask_b32_e64 v1, v1, v61, s[26:27]
	v_cndmask_b32_e64 v1, v1, v62, s[28:29]
	v_lshl_add_u32 v3, v0, 5, v63
	v_add_u32_e32 v3, v3, v1
	s_and_saveexec_b64 s[30:31], s[12:13]
	s_cbranch_execz .Lco_nold1
	global_load_dwordx4 v[212:215], v3, s[66:67] sc1
	global_load_dword v81, v3, s[66:67] offset:16 sc1
	v_mov_b32_e32 v19, 1.0
.Lco_nold1:
	s_mov_b64 exec, s[30:31]
	v_add_u32_e32 v0, 32, v70
	v_cmp_lt_u32_e64 s[12:13], v0, v52
	v_cmp_le_u32_e64 s[16:17], v45, v0
	v_cmp_le_u32_e64 s[18:19], v46, v0
	v_cmp_le_u32_e64 s[20:21], v47, v0
	v_cmp_le_u32_e64 s[22:23], v48, v0
	v_cmp_le_u32_e64 s[24:25], v49, v0
	v_cmp_le_u32_e64 s[26:27], v50, v0
	v_cmp_le_u32_e64 s[28:29], v51, v0
	v_cndmask_b32_e64 v1, 0, v56, s[16:17]
	v_cndmask_b32_e64 v1, v1, v57, s[18:19]
	v_cndmask_b32_e64 v1, v1, v58, s[20:21]
	v_cndmask_b32_e64 v1, v1, v59, s[22:23]
	v_cndmask_b32_e64 v1, v1, v60, s[24:25]
	v_cndmask_b32_e64 v1, v1, v61, s[26:27]
	v_cndmask_b32_e64 v1, v1, v62, s[28:29]
	v_lshl_add_u32 v4, v0, 5, v63
	v_add_u32_e32 v4, v4, v1
	s_and_saveexec_b64 s[30:31], s[12:13]
	s_cbranch_execz .Lco_nold2
	global_load_dwordx4 v[216:219], v4, s[66:67] sc1
	global_load_dword v85, v4, s[66:67] offset:16 sc1
	v_mov_b32_e32 v20, 1.0
.Lco_nold2:
	s_mov_b64 exec, s[30:31]
	v_add_u32_e32 v0, 48, v70
	v_cmp_lt_u32_e64 s[12:13], v0, v52
	v_cmp_le_u32_e64 s[16:17], v45, v0
	v_cmp_le_u32_e64 s[18:19], v46, v0
	v_cmp_le_u32_e64 s[20:21], v47, v0
	v_cmp_le_u32_e64 s[22:23], v48, v0
	v_cmp_le_u32_e64 s[24:25], v49, v0
	v_cmp_le_u32_e64 s[26:27], v50, v0
	v_cmp_le_u32_e64 s[28:29], v51, v0
	v_cndmask_b32_e64 v1, 0, v56, s[16:17]
	v_cndmask_b32_e64 v1, v1, v57, s[18:19]
	v_cndmask_b32_e64 v1, v1, v58, s[20:21]
	v_cndmask_b32_e64 v1, v1, v59, s[22:23]
	v_cndmask_b32_e64 v1, v1, v60, s[24:25]
	v_cndmask_b32_e64 v1, v1, v61, s[26:27]
	v_cndmask_b32_e64 v1, v1, v62, s[28:29]
	v_lshl_add_u32 v5, v0, 5, v63
	v_add_u32_e32 v5, v5, v1
	s_and_saveexec_b64 s[30:31], s[12:13]
	s_cbranch_execz .Lco_nold3
	global_load_dwordx4 v[220:223], v5, s[66:67] sc1
	global_load_dword v86, v5, s[66:67] offset:16 sc1
	v_mov_b32_e32 v21, 1.0
.Lco_nold3:
	s_mov_b64 exec, s[30:31]
	v_add_u32_e32 v0, 64, v70
	v_cmp_lt_u32_e64 s[12:13], v0, v52
	v_cmp_le_u32_e64 s[16:17], v45, v0
	v_cmp_le_u32_e64 s[18:19], v46, v0
	v_cmp_le_u32_e64 s[20:21], v47, v0
	v_cmp_le_u32_e64 s[22:23], v48, v0
	v_cmp_le_u32_e64 s[24:25], v49, v0
	v_cmp_le_u32_e64 s[26:27], v50, v0
	v_cmp_le_u32_e64 s[28:29], v51, v0
	v_cndmask_b32_e64 v1, 0, v56, s[16:17]
	v_cndmask_b32_e64 v1, v1, v57, s[18:19]
	v_cndmask_b32_e64 v1, v1, v58, s[20:21]
	v_cndmask_b32_e64 v1, v1, v59, s[22:23]
	v_cndmask_b32_e64 v1, v1, v60, s[24:25]
	v_cndmask_b32_e64 v1, v1, v61, s[26:27]
	v_cndmask_b32_e64 v1, v1, v62, s[28:29]
	v_lshl_add_u32 v6, v0, 5, v63
	v_add_u32_e32 v6, v6, v1
	s_and_saveexec_b64 s[30:31], s[12:13]
	s_cbranch_execz .Lco_nold4
	global_load_dwordx4 v[224:227], v6, s[66:67] sc1
	global_load_dword v87, v6, s[66:67] offset:16 sc1
	v_mov_b32_e32 v22, 1.0
.Lco_nold4:
	s_mov_b64 exec, s[30:31]
	v_add_u32_e32 v0, 80, v70
	v_cmp_lt_u32_e64 s[12:13], v0, v52
	v_cmp_le_u32_e64 s[16:17], v45, v0
	v_cmp_le_u32_e64 s[18:19], v46, v0
	v_cmp_le_u32_e64 s[20:21], v47, v0
	v_cmp_le_u32_e64 s[22:23], v48, v0
	v_cmp_le_u32_e64 s[24:25], v49, v0
	v_cmp_le_u32_e64 s[26:27], v50, v0
	v_cmp_le_u32_e64 s[28:29], v51, v0
	v_cndmask_b32_e64 v1, 0, v56, s[16:17]
	v_cndmask_b32_e64 v1, v1, v57, s[18:19]
	v_cndmask_b32_e64 v1, v1, v58, s[20:21]
	v_cndmask_b32_e64 v1, v1, v59, s[22:23]
	v_cndmask_b32_e64 v1, v1, v60, s[24:25]
	v_cndmask_b32_e64 v1, v1, v61, s[26:27]
	v_cndmask_b32_e64 v1, v1, v62, s[28:29]
	v_lshl_add_u32 v7, v0, 5, v63
	v_add_u32_e32 v7, v7, v1
	s_and_saveexec_b64 s[30:31], s[12:13]
	s_cbranch_execz .Lco_nold5
	global_load_dwordx4 v[228:231], v7, s[66:67] sc1
	global_load_dword v88, v7, s[66:67] offset:16 sc1
	v_mov_b32_e32 v23, 1.0
.Lco_nold5:
	s_mov_b64 exec, s[30:31]
	v_add_u32_e32 v0, 96, v70
	v_cmp_lt_u32_e64 s[12:13], v0, v52
	v_cmp_le_u32_e64 s[16:17], v45, v0
	v_cmp_le_u32_e64 s[18:19], v46, v0
	v_cmp_le_u32_e64 s[20:21], v47, v0
	v_cmp_le_u32_e64 s[22:23], v48, v0
	v_cmp_le_u32_e64 s[24:25], v49, v0
	v_cmp_le_u32_e64 s[26:27], v50, v0
	v_cmp_le_u32_e64 s[28:29], v51, v0
	v_cndmask_b32_e64 v1, 0, v56, s[16:17]
	v_cndmask_b32_e64 v1, v1, v57, s[18:19]
	v_cndmask_b32_e64 v1, v1, v58, s[20:21]
	v_cndmask_b32_e64 v1, v1, v59, s[22:23]
	v_cndmask_b32_e64 v1, v1, v60, s[24:25]
	v_cndmask_b32_e64 v1, v1, v61, s[26:27]
	v_cndmask_b32_e64 v1, v1, v62, s[28:29]
	v_lshl_add_u32 v10, v0, 5, v63
	v_add_u32_e32 v10, v10, v1
	s_and_saveexec_b64 s[30:31], s[12:13]
	s_cbranch_execz .Lco_nold6
	global_load_dwordx4 v[232:235], v10, s[66:67] sc1
	global_load_dword v89, v10, s[66:67] offset:16 sc1
	v_mov_b32_e32 v24, 1.0
.Lco_nold6:
	s_mov_b64 exec, s[30:31]
	v_add_u32_e32 v0, 112, v70
	v_cmp_lt_u32_e64 s[12:13], v0, v52
	v_cmp_le_u32_e64 s[16:17], v45, v0
	v_cmp_le_u32_e64 s[18:19], v46, v0
	v_cmp_le_u32_e64 s[20:21], v47, v0
	v_cmp_le_u32_e64 s[22:23], v48, v0
	v_cmp_le_u32_e64 s[24:25], v49, v0
	v_cmp_le_u32_e64 s[26:27], v50, v0
	v_cmp_le_u32_e64 s[28:29], v51, v0
	v_cndmask_b32_e64 v1, 0, v56, s[16:17]
	v_cndmask_b32_e64 v1, v1, v57, s[18:19]
	v_cndmask_b32_e64 v1, v1, v58, s[20:21]
	v_cndmask_b32_e64 v1, v1, v59, s[22:23]
	v_cndmask_b32_e64 v1, v1, v60, s[24:25]
	v_cndmask_b32_e64 v1, v1, v61, s[26:27]
	v_cndmask_b32_e64 v1, v1, v62, s[28:29]
	v_lshl_add_u32 v11, v0, 5, v63
	v_add_u32_e32 v11, v11, v1
	s_and_saveexec_b64 s[30:31], s[12:13]
	s_cbranch_execz .Lco_nold7
	global_load_dwordx4 v[236:239], v11, s[66:67] sc1
	global_load_dword v90, v11, s[66:67] offset:16 sc1
	v_mov_b32_e32 v25, 1.0
.Lco_nold7:
	s_mov_b64 exec, s[30:31]
	s_cmp_gt_i32 s77, 8
	s_cbranch_scc0 .Lco_ld_done
	v_add_u32_e32 v0, 128, v70
	v_cmp_lt_u32_e64 s[12:13], v0, v52
	v_cmp_le_u32_e64 s[16:17], v45, v0
	v_cmp_le_u32_e64 s[18:19], v46, v0
	v_cmp_le_u32_e64 s[20:21], v47, v0
	v_cmp_le_u32_e64 s[22:23], v48, v0
	v_cmp_le_u32_e64 s[24:25], v49, v0
	v_cmp_le_u32_e64 s[26:27], v50, v0
	v_cmp_le_u32_e64 s[28:29], v51, v0
	v_cndmask_b32_e64 v1, 0, v56, s[16:17]
	v_cndmask_b32_e64 v1, v1, v57, s[18:19]
	v_cndmask_b32_e64 v1, v1, v58, s[20:21]
	v_cndmask_b32_e64 v1, v1, v59, s[22:23]
	v_cndmask_b32_e64 v1, v1, v60, s[24:25]
	v_cndmask_b32_e64 v1, v1, v61, s[26:27]
	v_cndmask_b32_e64 v1, v1, v62, s[28:29]
	v_lshl_add_u32 v12, v0, 5, v63
	v_add_u32_e32 v12, v12, v1
	s_and_saveexec_b64 s[30:31], s[12:13]
	s_cbranch_execz .Lco_nold8
	global_load_dwordx4 v[240:243], v12, s[66:67] sc1
	global_load_dword v91, v12, s[66:67] offset:16 sc1
	v_mov_b32_e32 v26, 1.0
.Lco_nold8:
	s_mov_b64 exec, s[30:31]
	v_add_u32_e32 v0, 144, v70
	v_cmp_lt_u32_e64 s[12:13], v0, v52
	v_cmp_le_u32_e64 s[16:17], v45, v0
	v_cmp_le_u32_e64 s[18:19], v46, v0
	v_cmp_le_u32_e64 s[20:21], v47, v0
	v_cmp_le_u32_e64 s[22:23], v48, v0
	v_cmp_le_u32_e64 s[24:25], v49, v0
	v_cmp_le_u32_e64 s[26:27], v50, v0
	v_cmp_le_u32_e64 s[28:29], v51, v0
	v_cndmask_b32_e64 v1, 0, v56, s[16:17]
	v_cndmask_b32_e64 v1, v1, v57, s[18:19]
	v_cndmask_b32_e64 v1, v1, v58, s[20:21]
	v_cndmask_b32_e64 v1, v1, v59, s[22:23]
	v_cndmask_b32_e64 v1, v1, v60, s[24:25]
	v_cndmask_b32_e64 v1, v1, v61, s[26:27]
	v_cndmask_b32_e64 v1, v1, v62, s[28:29]
	v_lshl_add_u32 v13, v0, 5, v63
	v_add_u32_e32 v13, v13, v1
	s_and_saveexec_b64 s[30:31], s[12:13]
	s_cbranch_execz .Lco_nold9
	global_load_dwordx4 v[244:247], v13, s[66:67] sc1
	global_load_dword v92, v13, s[66:67] offset:16 sc1
	v_mov_b32_e32 v27, 1.0
.Lco_nold9:
	s_mov_b64 exec, s[30:31]
	s_cmp_gt_i32 s77, 10
	s_cbranch_scc0 .Lco_ld_done
	v_add_u32_e32 v0, 160, v70
	v_cmp_lt_u32_e64 s[12:13], v0, v52
	v_cmp_le_u32_e64 s[16:17], v45, v0
	v_cmp_le_u32_e64 s[18:19], v46, v0
	v_cmp_le_u32_e64 s[20:21], v47, v0
	v_cmp_le_u32_e64 s[22:23], v48, v0
	v_cmp_le_u32_e64 s[24:25], v49, v0
	v_cmp_le_u32_e64 s[26:27], v50, v0
	v_cmp_le_u32_e64 s[28:29], v51, v0
	v_cndmask_b32_e64 v1, 0, v56, s[16:17]
	v_cndmask_b32_e64 v1, v1, v57, s[18:19]
	v_cndmask_b32_e64 v1, v1, v58, s[20:21]
	v_cndmask_b32_e64 v1, v1, v59, s[22:23]
	v_cndmask_b32_e64 v1, v1, v60, s[24:25]
	v_cndmask_b32_e64 v1, v1, v61, s[26:27]
	v_cndmask_b32_e64 v1, v1, v62, s[28:29]
	v_lshl_add_u32 v14, v0, 5, v63
	v_add_u32_e32 v14, v14, v1
	s_and_saveexec_b64 s[30:31], s[12:13]
	s_cbranch_execz .Lco_nold10
	global_load_dwordx4 v[248:251], v14, s[66:67] sc1
	global_load_dword v93, v14, s[66:67] offset:16 sc1
	v_mov_b32_e32 v28, 1.0
.Lco_nold10:
	s_mov_b64 exec, s[30:31]
	v_add_u32_e32 v0, 176, v70
	v_cmp_lt_u32_e64 s[12:13], v0, v52
	v_cmp_le_u32_e64 s[16:17], v45, v0
	v_cmp_le_u32_e64 s[18:19], v46, v0
	v_cmp_le_u32_e64 s[20:21], v47, v0
	v_cmp_le_u32_e64 s[22:23], v48, v0
	v_cmp_le_u32_e64 s[24:25], v49, v0
	v_cmp_le_u32_e64 s[26:27], v50, v0
	v_cmp_le_u32_e64 s[28:29], v51, v0
	v_cndmask_b32_e64 v1, 0, v56, s[16:17]
	v_cndmask_b32_e64 v1, v1, v57, s[18:19]
	v_cndmask_b32_e64 v1, v1, v58, s[20:21]
	v_cndmask_b32_e64 v1, v1, v59, s[22:23]
	v_cndmask_b32_e64 v1, v1, v60, s[24:25]
	v_cndmask_b32_e64 v1, v1, v61, s[26:27]
	v_cndmask_b32_e64 v1, v1, v62, s[28:29]
	v_lshl_add_u32 v15, v0, 5, v63
	v_add_u32_e32 v15, v15, v1
	s_and_saveexec_b64 s[30:31], s[12:13]
	s_cbranch_execz .Lco_nold11
	global_load_dwordx4 v[164:167], v15, s[66:67] sc1
	global_load_dword v94, v15, s[66:67] offset:16 sc1
	v_mov_b32_e32 v29, 1.0
.Lco_nold11:
	s_mov_b64 exec, s[30:31]
	v_add_u32_e32 v0, 192, v70
	v_cmp_lt_u32_e64 s[12:13], v0, v52
	v_cmp_le_u32_e64 s[16:17], v45, v0
	v_cmp_le_u32_e64 s[18:19], v46, v0
	v_cmp_le_u32_e64 s[20:21], v47, v0
	v_cmp_le_u32_e64 s[22:23], v48, v0
	v_cmp_le_u32_e64 s[24:25], v49, v0
	v_cmp_le_u32_e64 s[26:27], v50, v0
	v_cmp_le_u32_e64 s[28:29], v51, v0
	v_cndmask_b32_e64 v1, 0, v56, s[16:17]
	v_cndmask_b32_e64 v1, v1, v57, s[18:19]
	v_cndmask_b32_e64 v1, v1, v58, s[20:21]
	v_cndmask_b32_e64 v1, v1, v59, s[22:23]
	v_cndmask_b32_e64 v1, v1, v60, s[24:25]
	v_cndmask_b32_e64 v1, v1, v61, s[26:27]
	v_cndmask_b32_e64 v1, v1, v62, s[28:29]
	v_lshl_add_u32 v35, v0, 5, v63
	v_add_u32_e32 v35, v35, v1
	s_and_saveexec_b64 s[30:31], s[12:13]
	s_cbranch_execz .Lco_nold12
	global_load_dwordx4 v[168:171], v35, s[66:67] sc1
	global_load_dword v95, v35, s[66:67] offset:16 sc1
	v_mov_b32_e32 v30, 1.0
.Lco_nold12:
	s_mov_b64 exec, s[30:31]
	v_add_u32_e32 v0, 208, v70
	v_cmp_lt_u32_e64 s[12:13], v0, v52
	v_cmp_le_u32_e64 s[16:17], v45, v0
	v_cmp_le_u32_e64 s[18:19], v46, v0
	v_cmp_le_u32_e64 s[20:21], v47, v0
	v_cmp_le_u32_e64 s[22:23], v48, v0
	v_cmp_le_u32_e64 s[24:25], v49, v0
	v_cmp_le_u32_e64 s[26:27], v50, v0
	v_cmp_le_u32_e64 s[28:29], v51, v0
	v_cndmask_b32_e64 v1, 0, v56, s[16:17]
	v_cndmask_b32_e64 v1, v1, v57, s[18:19]
	v_cndmask_b32_e64 v1, v1, v58, s[20:21]
	v_cndmask_b32_e64 v1, v1, v59, s[22:23]
	v_cndmask_b32_e64 v1, v1, v60, s[24:25]
	v_cndmask_b32_e64 v1, v1, v61, s[26:27]
	v_cndmask_b32_e64 v1, v1, v62, s[28:29]
	v_lshl_add_u32 v64, v0, 5, v63
	v_add_u32_e32 v64, v64, v1
	s_and_saveexec_b64 s[30:31], s[12:13]
	s_cbranch_execz .Lco_nold13
	global_load_dwordx4 v[172:175], v64, s[66:67] sc1
	global_load_dword v96, v64, s[66:67] offset:16 sc1
	v_mov_b32_e32 v31, 1.0
.Lco_nold13:
	s_mov_b64 exec, s[30:31]
	v_add_u32_e32 v0, 224, v70
	v_cmp_lt_u32_e64 s[12:13], v0, v52
	v_cmp_le_u32_e64 s[16:17], v45, v0
	v_cmp_le_u32_e64 s[18:19], v46, v0
	v_cmp_le_u32_e64 s[20:21], v47, v0
	v_cmp_le_u32_e64 s[22:23], v48, v0
	v_cmp_le_u32_e64 s[24:25], v49, v0
	v_cmp_le_u32_e64 s[26:27], v50, v0
	v_cmp_le_u32_e64 s[28:29], v51, v0
	v_cndmask_b32_e64 v1, 0, v56, s[16:17]
	v_cndmask_b32_e64 v1, v1, v57, s[18:19]
	v_cndmask_b32_e64 v1, v1, v58, s[20:21]
	v_cndmask_b32_e64 v1, v1, v59, s[22:23]
	v_cndmask_b32_e64 v1, v1, v60, s[24:25]
	v_cndmask_b32_e64 v1, v1, v61, s[26:27]
	v_cndmask_b32_e64 v1, v1, v62, s[28:29]
	v_lshl_add_u32 v65, v0, 5, v63
	v_add_u32_e32 v65, v65, v1
	s_and_saveexec_b64 s[30:31], s[12:13]
	s_cbranch_execz .Lco_nold14
	global_load_dwordx4 v[176:179], v65, s[66:67] sc1
	global_load_dword v97, v65, s[66:67] offset:16 sc1
	v_mov_b32_e32 v32, 1.0
.Lco_nold14:
	s_mov_b64 exec, s[30:31]
	v_add_u32_e32 v0, 240, v70
	v_cmp_lt_u32_e64 s[12:13], v0, v52
	v_cmp_le_u32_e64 s[16:17], v45, v0
	v_cmp_le_u32_e64 s[18:19], v46, v0
	v_cmp_le_u32_e64 s[20:21], v47, v0
	v_cmp_le_u32_e64 s[22:23], v48, v0
	v_cmp_le_u32_e64 s[24:25], v49, v0
	v_cmp_le_u32_e64 s[26:27], v50, v0
	v_cmp_le_u32_e64 s[28:29], v51, v0
	v_cndmask_b32_e64 v1, 0, v56, s[16:17]
	v_cndmask_b32_e64 v1, v1, v57, s[18:19]
	v_cndmask_b32_e64 v1, v1, v58, s[20:21]
	v_cndmask_b32_e64 v1, v1, v59, s[22:23]
	v_cndmask_b32_e64 v1, v1, v60, s[24:25]
	v_cndmask_b32_e64 v1, v1, v61, s[26:27]
	v_cndmask_b32_e64 v1, v1, v62, s[28:29]
	v_lshl_add_u32 v66, v0, 5, v63
	v_add_u32_e32 v66, v66, v1
	s_and_saveexec_b64 s[30:31], s[12:13]
	s_cbranch_execz .Lco_nold15
	global_load_dwordx4 v[180:183], v66, s[66:67] sc1
	global_load_dword v99, v66, s[66:67] offset:16 sc1
	v_mov_b32_e32 v33, 1.0
.Lco_nold15:
	s_mov_b64 exec, s[30:31]
.Lco_ld_done:
	s_waitcnt vmcnt(0)
	v_cmp_lt_u32_e64 s[12:13], v70, v52
	v_mov_b32_e32 v159, 0xf000
	s_nop 0
	s_and_saveexec_b64 s[30:31], s[12:13]
	v_mov_b32_e32 v159, v208
	v_mov_b32_e32 v9, v209
	v_mov_b32_e32 v129, v210
	v_mov_b32_e32 v130, v211
	s_mov_b64 exec, s[30:31]
	v_add_u32_e32 v0, 16, v70
	v_cmp_lt_u32_e64 s[12:13], v0, v52
	v_mov_b32_e32 v158, 0xf000
	s_nop 0
	s_and_saveexec_b64 s[30:31], s[12:13]
	v_mov_b32_e32 v158, v212
	v_mov_b32_e32 v131, v213
	v_mov_b32_e32 v132, v214
	v_mov_b32_e32 v133, v215
	s_mov_b64 exec, s[30:31]
	v_add_u32_e32 v0, 32, v70
	v_cmp_lt_u32_e64 s[12:13], v0, v52
	v_mov_b32_e32 v157, 0xf000
	s_nop 0
	s_and_saveexec_b64 s[30:31], s[12:13]
	v_mov_b32_e32 v157, v216
	v_mov_b32_e32 v134, v217
	v_mov_b32_e32 v135, v218
	v_mov_b32_e32 v136, v219
	s_mov_b64 exec, s[30:31]
	v_add_u32_e32 v0, 48, v70
	v_cmp_lt_u32_e64 s[12:13], v0, v52
	v_mov_b32_e32 v156, 0xf000
	s_nop 0
	s_and_saveexec_b64 s[30:31], s[12:13]
	v_mov_b32_e32 v156, v220
	v_mov_b32_e32 v137, v221
	v_mov_b32_e32 v138, v222
	v_mov_b32_e32 v139, v223
	s_mov_b64 exec, s[30:31]
	v_add_u32_e32 v0, 64, v70
	v_cmp_lt_u32_e64 s[12:13], v0, v52
	v_mov_b32_e32 v155, 0xf000
	s_nop 0
	s_and_saveexec_b64 s[30:31], s[12:13]
	v_mov_b32_e32 v155, v224
	v_mov_b32_e32 v140, v225
	v_mov_b32_e32 v141, v226
	v_mov_b32_e32 v142, v227
	s_mov_b64 exec, s[30:31]
	v_add_u32_e32 v0, 80, v70
	v_cmp_lt_u32_e64 s[12:13], v0, v52
	v_mov_b32_e32 v154, 0xf000
	s_nop 0
	s_and_saveexec_b64 s[30:31], s[12:13]
	v_mov_b32_e32 v154, v228
	v_mov_b32_e32 v143, v229
	v_mov_b32_e32 v144, v230
	v_mov_b32_e32 v145, v231
	s_mov_b64 exec, s[30:31]
	v_add_u32_e32 v0, 96, v70
	v_cmp_lt_u32_e64 s[12:13], v0, v52
	v_mov_b32_e32 v153, 0xf000
	s_nop 0
	s_and_saveexec_b64 s[30:31], s[12:13]
	v_mov_b32_e32 v153, v232
	v_mov_b32_e32 v146, v233
	v_mov_b32_e32 v147, v234
	v_mov_b32_e32 v148, v235
	s_mov_b64 exec, s[30:31]
	v_add_u32_e32 v0, 112, v70
	v_cmp_lt_u32_e64 s[12:13], v0, v52
	v_mov_b32_e32 v149, 0xf000
	s_nop 0
	s_and_saveexec_b64 s[30:31], s[12:13]
	v_mov_b32_e32 v149, v236
	v_mov_b32_e32 v150, v237
	v_mov_b32_e32 v151, v238
	v_mov_b32_e32 v152, v239
	s_mov_b64 exec, s[30:31]
	s_cmp_gt_i32 s77, 8
	s_cbranch_scc0 .Lco_done
	v_add_u32_e32 v0, 128, v70
	v_cmp_lt_u32_e64 s[12:13], v0, v52
	v_mov_b32_e32 v128, 0xf000
	s_nop 0
	s_and_saveexec_b64 s[30:31], s[12:13]
	v_mov_b32_e32 v128, v240
	v_mov_b32_e32 v121, v241
	v_mov_b32_e32 v123, v242
	v_mov_b32_e32 v125, v243
	s_mov_b64 exec, s[30:31]
	v_add_u32_e32 v0, 144, v70
	v_cmp_lt_u32_e64 s[12:13], v0, v52
	v_mov_b32_e32 v127, 0xf000
	s_nop 0
	s_and_saveexec_b64 s[30:31], s[12:13]
	v_mov_b32_e32 v127, v244
	v_mov_b32_e32 v122, v245
	v_mov_b32_e32 v124, v246
	v_mov_b32_e32 v126, v247
	s_mov_b64 exec, s[30:31]
	s_cmp_gt_i32 s77, 10
	s_cbranch_scc0 .Lco_done
	v_add_u32_e32 v0, 160, v70
	v_cmp_lt_u32_e64 s[12:13], v0, v52
	v_mov_b32_e32 v120, 0xf000
	s_nop 0
	s_and_saveexec_b64 s[30:31], s[12:13]
	v_mov_b32_e32 v120, v248
	v_mov_b32_e32 v112, v249
	v_mov_b32_e32 v115, v250
	v_mov_b32_e32 v117, v251
	s_mov_b64 exec, s[30:31]
	v_add_u32_e32 v0, 176, v70
	v_cmp_lt_u32_e64 s[12:13], v0, v52
	v_mov_b32_e32 v119, 0xf000
	s_nop 0
	s_and_saveexec_b64 s[30:31], s[12:13]
	v_mov_b32_e32 v119, v164
	v_mov_b32_e32 v113, v165
	v_mov_b32_e32 v116, v166
	v_mov_b32_e32 v118, v167
	s_mov_b64 exec, s[30:31]
	v_add_u32_e32 v0, 192, v70
	v_cmp_lt_u32_e64 s[12:13], v0, v52
	v_mov_b32_e32 v114, 0xf000
	s_nop 0
	s_and_saveexec_b64 s[30:31], s[12:13]
	v_mov_b32_e32 v114, v168
	v_mov_b32_e32 v100, v169
	v_mov_b32_e32 v103, v170
	v_mov_b32_e32 v107, v171
	s_mov_b64 exec, s[30:31]
	v_add_u32_e32 v0, 208, v70
	v_cmp_lt_u32_e64 s[12:13], v0, v52
	v_mov_b32_e32 v111, 0xf000
	s_nop 0
	s_and_saveexec_b64 s[30:31], s[12:13]
	v_mov_b32_e32 v111, v172
	v_mov_b32_e32 v101, v173
	v_mov_b32_e32 v104, v174
	v_mov_b32_e32 v108, v175
	s_mov_b64 exec, s[30:31]
	v_add_u32_e32 v0, 224, v70
	v_cmp_lt_u32_e64 s[12:13], v0, v52
	v_mov_b32_e32 v17, 0xf000
	s_nop 0
	s_and_saveexec_b64 s[30:31], s[12:13]
	v_mov_b32_e32 v17, v176
	v_mov_b32_e32 v102, v177
	v_mov_b32_e32 v105, v178
	v_mov_b32_e32 v109, v179
	s_mov_b64 exec, s[30:31]
	v_add_u32_e32 v0, 240, v70
	v_cmp_lt_u32_e64 s[12:13], v0, v52
	v_mov_b32_e32 v8, 0xf000
	s_nop 0
	s_and_saveexec_b64 s[30:31], s[12:13]
	v_mov_b32_e32 v8, v180
	v_mov_b32_e32 v16, v181
	v_mov_b32_e32 v106, v182
	v_mov_b32_e32 v110, v183
	s_mov_b64 exec, s[30:31]
	s_branch .Lco_done
.Lco_gen:
	v_lshl_or_b32 v0, s78, 4, v75
	v_lshlrev_b32_e32 v0, 11, v0
	v_lshl_add_u32 v0, v70, 2, v0
	v_mov_b32_e32 v1, 1.0
	s_mov_b32 s37, 0
.Lco_wg:
	global_store_dword v0, v1, s[72:73]
	v_add_u32_e32 v0, 64, v0
	s_add_i32 s37, s37, 1
	s_cmp_lt_u32 s37, 32
	s_cbranch_scc1 .Lco_wg
.Lco_done:
	s_waitcnt vmcnt(0)
	s_mov_b64 s[44:45], exec

.Lk_318:
	v_mul_f32_e32 v250, v129, v229
	v_cmp_class_f32_e64 s[82:83], v228, 64
	v_add_f32_dpp v12, v180, v180 row_ror:8 row_mask:0xf bank_mask:0xf bound_ctrl:1
	v_mov_b32_e32 v61, v13
	v_cndmask_b32_e64 v46, v176, 5, s[16:17]
	v_mul_f32_e32 v251, v132, v231
	v_cmp_class_f32_e64 s[84:85], v230, 64
	v_add_f32_dpp v12, v12, v12 row_ror:4 row_mask:0xf bank_mask:0xf bound_ctrl:1
	s_mov_b64 s[60:61], s[16:17]
	v_fma_f32 v18, v250, v54, v18
	v_fma_f32 v19, v251, v54, v19
	v_cndmask_b32_e64 v250, -v130, v173, s[82:83]
	v_add_f32_dpp v60, v12, v12 row_ror:2 row_mask:0xf bank_mask:0xf bound_ctrl:1
	v_mov_b32_e32 v12, 48
	v_cndmask_b32_e64 v251, -v133, v173, s[84:85]
	v_fmac_f32_e32 v18, v250, v55
	v_fmac_f32_e32 v19, v251, v55
	v_mov_b32_dpp v61, v60 row_ror:1 row_mask:0xf bank_mask:0xf
	s_and_saveexec_b64 s[58:59], s[10:11]
	s_cbranch_execz .Lk_286
	v_med3_f32 v18, v18, v71, 0
	v_med3_f32 v19, v19, v81, 0
	v_add_f32_e32 v12, v60, v61
	v_cvt_f64_f32_e32 v[248:249], v12
	v_mul_f32_e32 v218, v9, v18
	v_mul_f32_e32 v219, v131, v19
	v_mul_f32_e32 v250, v135, v233
	v_fmac_f64_e32 v[248:249], v[0:1], v[10:11]
	v_cmp_gt_i32_e32 vcc, 1, v46
	v_mov_b32_e32 v12, 0
	v_cmp_class_f32_e64 s[82:83], v232, 64
	v_mul_f32_e32 v251, v138, v235
	v_cmp_class_f32_e64 s[84:85], v234, 64
	v_fma_f32 v20, v250, v54, v20
	v_cndmask_b32_e32 v1, 0, v249, vcc
	v_cndmask_b32_e32 v0, 0, v248, vcc
	s_waitcnt lgkmcnt(0)
	v_cvt_f64_f32_e32 v[248:249], v179
	v_fma_f32 v21, v251, v54, v21
	v_cndmask_b32_e64 v250, -v136, v173, s[82:83]
	v_cndmask_b32_e64 v251, -v139, v173, s[84:85]
	v_add_f64 v[0:1], v[0:1], v[248:249]
	v_fmac_f32_e32 v20, v250, v55
	v_fmac_f32_e32 v21, v251, v55
	v_med3_f32 v20, v20, v85, 0
	v_med3_f32 v21, v21, v86, 0
	v_cmp_le_f64_e32 vcc, 1.0, v[0:1]
	v_mul_f32_e32 v220, v134, v20
	v_mul_f32_e32 v221, v137, v21
	v_mul_f32_e32 v250, v141, v237
	v_cmp_class_f32_e64 s[82:83], v236, 64
	s_lshr_b32 s11, vcc_lo, 15
	s_and_b32 s10, vcc_lo, 1
	s_and_b32 s11, s11, 2
	s_or_b32 s60, s11, s10
	s_lshr_b64 s[10:11], vcc, 30
	s_and_b32 s10, s10, 4
	s_lshr_b32 s11, vcc_hi, 13
	s_or_b32 s10, s60, s10
	s_and_b32 s11, s11, 8
	s_or_b32 s10, s10, s11
	v_lshlrev_b32_e64 v248, v163, s10
	s_and_saveexec_b64 s[10:11], s[4:5]
	v_and_b32_e32 v12, 3, v178
	v_lshl_or_b32 v12, v12, 2, v175
	v_or_b32_e32 v249, 0x10000, v248
	ds_add_rtn_u32 v12, v12, v249
	s_or_b64 exec, exec, s[10:11]
	v_mul_f32_e32 v251, v144, v239
	v_cmp_class_f32_e64 s[84:85], v238, 64
	v_fma_f32 v22, v250, v54, v22
	v_fma_f32 v23, v251, v54, v23
	v_cndmask_b32_e64 v250, -v142, v173, s[82:83]
	v_cndmask_b32_e64 v251, -v145, v173, s[84:85]
	v_fmac_f32_e32 v22, v250, v55
	v_fmac_f32_e32 v23, v251, v55
	v_med3_f32 v22, v22, v87, 0
	v_med3_f32 v23, v23, v88, 0
	v_mul_f32_e32 v222, v140, v22
	v_mul_f32_e32 v223, v143, v23
	v_mul_f32_e32 v250, v147, v241
	v_cmp_class_f32_e64 s[82:83], v240, 64
	v_mul_f32_e32 v251, v151, v243
	v_cmp_class_f32_e64 s[84:85], v242, 64
	v_fma_f32 v24, v250, v54, v24
	v_fma_f32 v25, v251, v54, v25
	v_cndmask_b32_e64 v250, -v148, v173, s[82:83]
	v_cndmask_b32_e64 v251, -v152, v173, s[84:85]
	v_fmac_f32_e32 v24, v250, v55
	v_fmac_f32_e32 v25, v251, v55
	v_med3_f32 v24, v24, v89, 0
	v_med3_f32 v25, v25, v90, 0
	v_mul_f32_e32 v224, v146, v24
	v_mul_f32_e32 v225, v150, v25
	v_add_u16_e32 v208, 0x1000, v208
	v_add_u16_e32 v209, 0x1000, v209
	v_add_u16_e32 v210, 0x1000, v210
	v_add_u16_e32 v211, 0x1000, v211
	v_add_u16_e32 v212, 0x1000, v212
	v_add_u16_e32 v213, 0x1000, v213
	v_add_u16_e32 v214, 0x1000, v214
	v_add_u16_e32 v215, 0x1000, v215
	s_cmp_eq_u64 s[18:19], 0
	s_cbranch_scc1 .Lmy_no89
	v_mul_f32_e32 v250, v123, v245
	v_cmp_class_f32_e64 s[82:83], v244, 64
	v_mul_f32_e32 v251, v124, v247
	v_cmp_class_f32_e64 s[84:85], v246, 64
	v_fma_f32 v26, v250, v54, v26
	v_fma_f32 v27, v251, v54, v27
	v_cndmask_b32_e64 v250, -v125, v173, s[82:83]
	v_cndmask_b32_e64 v251, -v126, v173, s[84:85]
	v_fmac_f32_e32 v26, v250, v55
	v_fmac_f32_e32 v27, v251, v55
	v_med3_f32 v26, v26, v91, 0
	v_med3_f32 v27, v27, v92, 0
	v_mul_f32_e32 v226, v121, v26
	v_mul_f32_e32 v227, v122, v27
	v_add_u16_e32 v216, 0x1000, v216
	v_add_u16_e32 v217, 0x1000, v217
